# P1 log-f epilogue: the eight lower-bound-logit quads of a unit fetched at one site (4 load-wait round trips -> 1)
# speedup vs baseline: 1.0008x; 1.0008x over previous
;     DI void operator()(const f32x4 (&acc)[2][2][4][2], const pg8::Unit& u, int wr, int wc, int fr, int fq) const {
;     ...
;                 float lb[8];
;                 if (mode == 1) {
; #pragma unroll
;                     for (int e = 0; e < 8; ++e) lb[e] = 1.0f / (1.0f + __expf(lbl[2048 + col + e] - lbl[col + e]));
;                 }
.LBB0_188:
	v_lshl_or_b32 v162, v3, 8, v173
	s_xor_b64 s[16:17], s[4:5], -1
	v_ashrrev_i32_e32 v163, 31, v162
	s_and_b64 vcc, exec, s[16:17]
	v_lshl_add_u64 v[160:161], v[162:163], 2, s[20:21]
	s_cbranch_vccnz .LBB0_190
	v_add_co_u32_e32 v4, vcc, 0x2000, v160
	v_lshl_add_u64 v[168:169], v[160:161], 0, s[36:37]
	s_nop 0
	v_addc_co_u32_e32 v5, vcc, 0, v161, vcc
	global_load_dwordx4 v[4:7], v[4:5], off
	s_nop 0
	global_load_dwordx4 v[8:11], v[160:161], off
	global_load_dwordx4 v[164:167], v[160:161], off offset:16
	global_load_dwordx4 v[240:243], v[168:169], off offset:16
	v_lshl_add_u64 v[244:245], v[160:161], 0, s[46:47]
	global_load_dwordx4 v[224:227], v[244:245], off
	global_load_dwordx4 v[228:231], v[160:161], off offset:512
	global_load_dwordx4 v[232:235], v[160:161], off offset:528
	global_load_dwordx4 v[236:239], v[244:245], off offset:16
	s_waitcnt vmcnt(0)
	v_sub_f32_e32 v3, v4, v8
	v_sub_f32_e32 v4, v5, v9
	v_sub_f32_e32 v5, v6, v10
	v_sub_f32_e32 v6, v7, v11
	v_mul_f32_e32 v11, 0x3fb8aa3b, v4
	v_mul_f32_e32 v159, 0x3fb8aa3b, v5
	v_exp_f32_e32 v5, v11
	v_mul_f32_e32 v3, 0x3fb8aa3b, v3
	v_exp_f32_e32 v4, v3
	v_sub_f32_e32 v9, v242, v166
	v_sub_f32_e32 v10, v243, v167
	v_sub_f32_e32 v7, v240, v164
	v_mul_f32_e32 v167, 0x3fb8aa3b, v9
	v_mul_f32_e32 v168, 0x3fb8aa3b, v10
	v_sub_f32_e32 v8, v241, v165
	v_exp_f32_e32 v10, v167
	v_exp_f32_e32 v11, v168
	v_mul_f32_e32 v165, 0x3fb8aa3b, v7
	v_mul_f32_e32 v166, 0x3fb8aa3b, v8
	v_exp_f32_e32 v8, v165
	v_exp_f32_e32 v9, v166
	v_pk_add_f32 v[10:11], v[10:11], 1.0 op_sel_hi:[1,0]
	v_mul_f32_e32 v164, 0x3fb8aa3b, v6
	v_div_scale_f32 v3, s[4:5], v11, v11, 1.0
	v_exp_f32_e32 v7, v164
	v_pk_add_f32 v[8:9], v[8:9], 1.0 op_sel_hi:[1,0]
	v_div_scale_f32 v164, s[4:5], v10, v10, 1.0
	v_rcp_f32_e32 v180, v3
	v_div_scale_f32 v166, s[6:7], v9, v9, 1.0
	v_rcp_f32_e32 v181, v164
	v_exp_f32_e32 v6, v159
	v_div_scale_f32 v168, s[10:11], v8, v8, 1.0
	v_rcp_f32_e32 v182, v166
	v_rcp_f32_e32 v183, v168
	v_fma_f32 v185, -v3, v180, 1.0
	v_div_scale_f32 v159, vcc, 1.0, v11, 1.0
	v_fma_f32 v186, -v164, v181, 1.0
	v_fmac_f32_e32 v180, v185, v180
	v_pk_add_f32 v[6:7], v[6:7], 1.0 op_sel_hi:[1,0]
	v_div_scale_f32 v165, s[4:5], 1.0, v10, 1.0
	v_fma_f32 v187, -v166, v182, 1.0
	v_fmac_f32_e32 v181, v186, v181
	v_mul_f32_e32 v185, v159, v180
	v_div_scale_f32 v167, s[6:7], 1.0, v9, 1.0
	v_div_scale_f32 v170, s[12:13], v7, v7, 1.0
	v_fma_f32 v188, -v168, v183, 1.0
	v_fmac_f32_e32 v182, v187, v182
	v_mul_f32_e32 v186, v165, v181
	v_fma_f32 v190, -v3, v185, v159
	v_div_scale_f32 v169, s[10:11], 1.0, v8, 1.0
	v_rcp_f32_e32 v184, v170
	v_fmac_f32_e32 v183, v188, v183
	v_mul_f32_e32 v187, v167, v182
	v_fma_f32 v191, -v164, v186, v165
	v_fmac_f32_e32 v185, v190, v180
	v_mul_f32_e32 v188, v169, v183
	v_fma_f32 v192, -v166, v187, v167
	v_fmac_f32_e32 v186, v191, v181
	v_fma_f32 v3, -v3, v185, v159
	v_fma_f32 v193, -v168, v188, v169
	v_fmac_f32_e32 v187, v192, v182
	v_fma_f32 v159, -v164, v186, v165
	v_div_fmas_f32 v3, v3, v180, v185
	s_mov_b64 vcc, s[4:5]
	v_fmac_f32_e32 v188, v193, v183
	v_fma_f32 v164, -v166, v187, v167
	v_div_fixup_f32 v11, v3, v11, 1.0
	v_div_fmas_f32 v3, v159, v181, v186
	s_mov_b64 vcc, s[6:7]
	v_fma_f32 v189, -v170, v184, 1.0
	v_fma_f32 v165, -v168, v188, v169
	v_div_fixup_f32 v10, v3, v10, 1.0
	v_div_fmas_f32 v3, v164, v182, v187
	s_mov_b64 vcc, s[10:11]
	v_div_scale_f32 v171, s[12:13], 1.0, v7, 1.0
	v_fmac_f32_e32 v184, v189, v184
	v_div_fixup_f32 v9, v3, v9, 1.0
	v_div_fmas_f32 v3, v165, v183, v188
	v_mul_f32_e32 v189, v171, v184
	v_div_fixup_f32 v8, v3, v8, 1.0
	v_div_scale_f32 v3, s[4:5], v6, v6, 1.0
	v_fma_f32 v194, -v170, v189, v171
	v_rcp_f32_e32 v159, v3
	v_fmac_f32_e32 v189, v194, v184
	v_fma_f32 v166, -v170, v189, v171
	s_mov_b64 vcc, s[12:13]
	v_div_fmas_f32 v164, v166, v184, v189
	v_div_fixup_f32 v7, v164, v7, 1.0
	v_fma_f32 v164, -v3, v159, 1.0
	v_fmac_f32_e32 v159, v164, v159
	v_div_scale_f32 v164, vcc, 1.0, v6, 1.0
	v_mul_f32_e32 v165, v164, v159
	v_fma_f32 v166, -v3, v165, v164
	v_pk_add_f32 v[4:5], v[4:5], 1.0 op_sel_hi:[1,0]
	v_fmac_f32_e32 v165, v166, v159
	v_fma_f32 v3, -v3, v165, v164
	v_div_scale_f32 v164, s[4:5], v5, v5, 1.0
	v_rcp_f32_e32 v166, v164
	v_div_fmas_f32 v3, v3, v159, v165
	v_div_fixup_f32 v6, v3, v6, 1.0
	v_fma_f32 v3, -v164, v166, 1.0
	v_fmac_f32_e32 v166, v3, v166
	v_div_scale_f32 v3, vcc, 1.0, v5, 1.0
	v_mul_f32_e32 v159, v3, v166
	v_fma_f32 v165, -v164, v159, v3
	v_fmac_f32_e32 v159, v165, v166
	v_fma_f32 v3, -v164, v159, v3
	v_div_scale_f32 v164, s[4:5], v4, v4, 1.0
	v_rcp_f32_e32 v165, v164
	v_div_fmas_f32 v3, v3, v166, v159
	v_div_fixup_f32 v5, v3, v5, 1.0
	v_fma_f32 v3, -v164, v165, 1.0
	v_fmac_f32_e32 v165, v3, v165
	v_div_scale_f32 v3, vcc, 1.0, v4, 1.0
	v_mul_f32_e32 v159, v3, v165
	v_fma_f32 v166, -v164, v159, v3
	v_fmac_f32_e32 v159, v166, v165
	v_fma_f32 v3, -v164, v159, v3
	v_div_fmas_f32 v3, v3, v165, v159
	v_div_fixup_f32 v4, v3, v4, 1.0
	s_branch .LBB0_191

;     DI void operator()(const f32x4 (&acc)[2][2][4][2], const pg8::Unit& u, int wr, int wc, int fr, int fq) const {
;     ...
;                 float lb[8];
;                 if (mode == 1) {
; #pragma unroll
;                     for (int e = 0; e < 8; ++e) lb[e] = 1.0f / (1.0f + __expf(lbl[2048 + col + e] - lbl[col + e]));
;                 }
.LBB0_236:
	v_add_co_u32_e32 v4, vcc, 0x2000, v160
	v_lshl_add_u64 v[86:87], v[160:161], 0, s[46:47]
	s_nop 0
	v_addc_co_u32_e32 v5, vcc, 0, v161, vcc
	s_nop 0
	v_sub_f32_e32 v3, v224, v228
	v_sub_f32_e32 v4, v225, v229
	v_sub_f32_e32 v5, v226, v230
	v_sub_f32_e32 v6, v227, v231
	v_mul_f32_e32 v11, 0x3fb8aa3b, v4
	v_mul_f32_e32 v3, 0x3fb8aa3b, v3
	v_exp_f32_e32 v4, v3
	v_sub_f32_e32 v9, v238, v234
	v_sub_f32_e32 v10, v239, v235
	v_sub_f32_e32 v7, v236, v232
	v_sub_f32_e32 v8, v237, v233
	v_mul_f32_e32 v86, 0x3fb8aa3b, v9
	v_mul_f32_e32 v87, 0x3fb8aa3b, v10
	v_mul_f32_e32 v80, 0x3fb8aa3b, v5
	v_exp_f32_e32 v5, v11
	v_exp_f32_e32 v10, v86
	v_exp_f32_e32 v11, v87
	v_mul_f32_e32 v82, 0x3fb8aa3b, v7
	v_mul_f32_e32 v83, 0x3fb8aa3b, v8
	v_exp_f32_e32 v8, v82
	v_exp_f32_e32 v9, v83
	v_pk_add_f32 v[10:11], v[10:11], 1.0 op_sel_hi:[1,0]
	v_mul_f32_e32 v81, 0x3fb8aa3b, v6
	v_div_scale_f32 v3, s[10:11], v11, v11, 1.0
	v_exp_f32_e32 v7, v81
	v_pk_add_f32 v[8:9], v[8:9], 1.0 op_sel_hi:[1,0]
	v_div_scale_f32 v81, s[10:11], v10, v10, 1.0
	v_rcp_f32_e32 v91, v3
	v_div_scale_f32 v83, s[12:13], v9, v9, 1.0
	v_rcp_f32_e32 v94, v81
	v_exp_f32_e32 v6, v80
	v_div_scale_f32 v87, s[14:15], v8, v8, 1.0
	v_rcp_f32_e32 v95, v83
	v_rcp_f32_e32 v96, v87
	v_fma_f32 v98, -v3, v91, 1.0
	v_div_scale_f32 v80, vcc, 1.0, v11, 1.0
	v_fma_f32 v99, -v81, v94, 1.0
	v_fmac_f32_e32 v91, v98, v91
	v_pk_add_f32 v[6:7], v[6:7], 1.0 op_sel_hi:[1,0]
	v_div_scale_f32 v82, s[10:11], 1.0, v10, 1.0
	v_fma_f32 v102, -v83, v95, 1.0
	v_fmac_f32_e32 v94, v99, v94
	v_mul_f32_e32 v98, v80, v91
	v_div_scale_f32 v86, s[12:13], 1.0, v9, 1.0
	v_div_scale_f32 v89, s[16:17], v7, v7, 1.0
	v_fma_f32 v103, -v87, v96, 1.0
	v_fmac_f32_e32 v95, v102, v95
	v_mul_f32_e32 v99, v82, v94
	v_fma_f32 v105, -v3, v98, v80
	v_div_scale_f32 v88, s[14:15], 1.0, v8, 1.0
	v_rcp_f32_e32 v97, v89
	v_fmac_f32_e32 v96, v103, v96
	v_mul_f32_e32 v102, v86, v95
	v_fma_f32 v106, -v81, v99, v82
	v_fmac_f32_e32 v98, v105, v91
	v_mul_f32_e32 v103, v88, v96
	v_fma_f32 v107, -v83, v102, v86
	v_fmac_f32_e32 v99, v106, v94
	v_fma_f32 v3, -v3, v98, v80
	v_fma_f32 v110, -v87, v103, v88
	v_fmac_f32_e32 v102, v107, v95
	v_fma_f32 v80, -v81, v99, v82
	v_div_fmas_f32 v3, v3, v91, v98
	s_mov_b64 vcc, s[10:11]
	v_fmac_f32_e32 v103, v110, v96
	v_fma_f32 v81, -v83, v102, v86
	v_div_fixup_f32 v11, v3, v11, 1.0
	v_div_fmas_f32 v3, v80, v94, v99
	s_mov_b64 vcc, s[12:13]
	v_fma_f32 v104, -v89, v97, 1.0
	v_fma_f32 v82, -v87, v103, v88
	v_div_fixup_f32 v10, v3, v10, 1.0
	v_div_fmas_f32 v3, v81, v95, v102
	s_mov_b64 vcc, s[14:15]
	v_div_scale_f32 v90, s[16:17], 1.0, v7, 1.0
	v_fmac_f32_e32 v97, v104, v97
	v_div_fixup_f32 v9, v3, v9, 1.0
	v_div_fmas_f32 v3, v82, v96, v103
	v_mul_f32_e32 v104, v90, v97
	v_div_fixup_f32 v8, v3, v8, 1.0
	v_div_scale_f32 v3, s[10:11], v6, v6, 1.0
	v_fma_f32 v111, -v89, v104, v90
	v_rcp_f32_e32 v80, v3
	v_fmac_f32_e32 v104, v111, v97
	v_fma_f32 v83, -v89, v104, v90
	s_mov_b64 vcc, s[16:17]
	v_div_fmas_f32 v81, v83, v97, v104
	v_div_fixup_f32 v7, v81, v7, 1.0
	v_fma_f32 v81, -v3, v80, 1.0
	v_fmac_f32_e32 v80, v81, v80
	v_div_scale_f32 v81, vcc, 1.0, v6, 1.0
	v_mul_f32_e32 v82, v81, v80
	v_fma_f32 v83, -v3, v82, v81
	v_pk_add_f32 v[4:5], v[4:5], 1.0 op_sel_hi:[1,0]
	v_fmac_f32_e32 v82, v83, v80
	v_fma_f32 v3, -v3, v82, v81
	v_div_scale_f32 v81, s[10:11], v5, v5, 1.0
	v_rcp_f32_e32 v83, v81
	v_div_fmas_f32 v3, v3, v80, v82
	v_div_fixup_f32 v6, v3, v6, 1.0
	v_fma_f32 v3, -v81, v83, 1.0
	v_fmac_f32_e32 v83, v3, v83
	v_div_scale_f32 v3, vcc, 1.0, v5, 1.0
	v_mul_f32_e32 v80, v3, v83
	v_fma_f32 v82, -v81, v80, v3
	v_fmac_f32_e32 v80, v82, v83
	v_fma_f32 v3, -v81, v80, v3
	v_div_scale_f32 v81, s[10:11], v4, v4, 1.0
	v_rcp_f32_e32 v82, v81
	v_div_fmas_f32 v3, v3, v83, v80
	v_div_fixup_f32 v5, v3, v5, 1.0
	v_fma_f32 v3, -v81, v82, 1.0
	v_fmac_f32_e32 v82, v3, v82
	v_div_scale_f32 v3, vcc, 1.0, v4, 1.0
	v_mul_f32_e32 v80, v3, v82
	v_fma_f32 v83, -v81, v80, v3
	v_fmac_f32_e32 v80, v83, v82
	v_fma_f32 v3, -v81, v80, v3
	v_div_fmas_f32 v3, v3, v82, v80
	v_div_fixup_f32 v4, v3, v4, 1.0
